# adds exact counted vmcnt waits at the P4 chunk-prep loop header (was vmcnt(1)/vmcnt(0) draining the previous unit's stores)
# speedup vs baseline: 1.0082x; 1.0082x over previous
; #define LAS __attribute__((address_space(3)))
; __device__ __forceinline__ void p3_prep(Frame& F) {
;     ...
;     const int tid = tz, lane = tz & 63, w = __builtin_amdgcn_readfirstlane(tz >> 6), l15 = lane & 15, l4 = lane >> 4, r31 = lane & 31, hh = lane >> 5;
;     u32x4 pre[3][2]; float pg = 0.f, pb = 0.f;
;     ...
;     if (F.bid < NUNITS) PREP_LOAD(F.bid);
;     for (int uid = F.bid; uid < NUNITS; uid += F.G) {
;         unsigned char* ub = F.ws + WS_PREP + (size_t)uid * UNIT_BYTES;
;         float gc = pg; const float beta = pb;
; #pragma unroll
;         for (int off = 1; off < 64; off <<= 1) { const float t = __shfl_up(gc, off); if (lane >= off) gc += t; }
;         const float glast = __shfl(gc, 63), egcv = __expf(gc);
;         if (w == 0) { egc_s[lane] = egcv; ekd_s[lane] = __expf(glast - gc); gc_s[lane] = gc; beta_s[lane] = beta; }
;         { const int r0 = 2 * (tid >> 4), c16 = tid & 15;
;           const float br0 = __shfl(beta, r0), br1 = __shfl(beta, r0 + 1), sk0 = br0 * __shfl(egcv, r0), sk1 = br1 * __shfl(egcv, r0 + 1);
;           const int rs = (((r0 >> 3) ^ (c16 >> 1)) << 3) + (r0 & 7);
;           *(LAS u32x4*)(Qs + r0 * QP + c16 * 8) = pre[0][0]; *(LAS u32x4*)(Qs + (r0 + 1) * QP + c16 * 8) = pre[0][1];
;           *(LAS u32x4*)(Ks + r0 * QP + c16 * 8) = pre[1][0]; *(LAS u32x4*)(Ks + (r0 + 1) * QP + c16 * 8) = pre[1][1];
; #pragma unroll
;           for (int e = 0; e < 4; ++e) { const unsigned k0 = pre[1][0][e], k1 = pre[1][1][e], v0 = pre[2][0][e], v1 = pre[2][1][e];
;               *(LAS unsigned*)(KbgT + (c16 * 8 + 2 * e) * TP + rs) = pk(bf_lo(k0) * sk0, bf_lo(k1) * sk1); *(LAS unsigned*)(KbgT + (c16 * 8 + 2 * e + 1) * TP + rs) = pk(bf_hi(k0) * sk0, bf_hi(k1) * sk1);
;               *(LAS unsigned*)(VbT + (c16 * 8 + 2 * e) * TP + rs) = pk(bf_lo(v0) * br0, bf_lo(v1) * br1); *(LAS unsigned*)(VbT + (c16 * 8 + 2 * e + 1) * TP + rs) = pk(bf_hi(v0) * br0, bf_hi(v1) * br1); } }
;         if (uid + F.G < NUNITS) PREP_LOAD(uid + F.G);
;         __syncthreads();
;         { const bool isq = w >= 4; const int rt = w & 3; const LAS bf16_t* X = isq ? Qs : Ks; LAS float* OUT = isq ? QKm : Am;
;           bf16x8 af[4], bfr[4][4];
; #pragma unroll
;           for (int ks = 0; ks < 4; ++ks) af[ks] = *(const LAS bf16x8*)(X + (rt * 16 + l15) * QP + 32 * ks + 8 * l4);
; #pragma unroll
;           for (int st = 0; st < 4; ++st)
; #pragma unroll
.LBB0_485:
	v_writelane_b32 v254, s12, 40
	s_mov_b32 s3, 0
	s_ashr_i32 s16, s20, 6
	v_writelane_b32 v254, s13, 41
	v_writelane_b32 v254, s2, 14
	v_and_b32_e32 v117, 15, v26
	v_mbcnt_lo_u32_b32 v28, -1, 0
	v_writelane_b32 v254, s3, 15
	s_add_i32 s3, 0, 0x1c600
	s_cmp_lt_u32 s20, 64
	s_cselect_b64 s[4:5], -1, 0
	v_writelane_b32 v254, s4, 16
	s_add_i32 s6, 0, 0x1c500
	s_add_i32 s2, 0, 0x1c400
	v_writelane_b32 v254, s5, 17
	s_add_i32 s4, 0, 0x20b00
	s_add_i32 s5, 0, 0x20a00
	s_and_b32 s7, s16, 3
	s_add_i32 s8, 0, 0x4400
	s_add_i32 s9, 0, 0x15c00
	s_add_i32 s10, 0, 0x11800
	v_lshlrev_b32_e32 v102, 4, v117
	v_mov_b32_e32 v103, 0
	s_cmp_lt_i32 s16, 4
	v_mbcnt_hi_u32_b32 v37, -1, v28
	v_lshl_add_u64 v[104:105], s[0:1], 0, v[102:103]
	s_cselect_b64 s[0:1], -1, 0
	v_and_b32_e32 v38, 64, v37
	v_bfrev_b32_e32 v28, 0.5
	v_writelane_b32 v253, s0, 47
	s_cmp_gt_i32 s16, 3
	v_lshl_or_b32 v118, v37, 2, v28
	v_and_or_b32 v28, v27, 62, v38
	v_or_b32_e32 v125, 1, v27
	v_writelane_b32 v253, s1, 48
	s_cselect_b64 s[0:1], -1, 0
	v_lshlrev_b32_e32 v124, 2, v28
	v_and_or_b32 v28, v125, 63, v38
	v_writelane_b32 v253, s0, 34
	v_and_b32_e32 v123, -2, v27
	v_lshlrev_b32_e32 v126, 2, v28
	v_ashrrev_i32_e32 v28, 6, v26
	v_bfe_u32 v29, v26, 1, 3
	s_movk_i32 s14, 0x110
	v_lshlrev_b32_e32 v27, 1, v27
	v_writelane_b32 v253, s1, 35
	s_and_b64 s[0:1], s[0:1], exec
	v_xor_b32_e32 v28, v29, v28
	v_mul_lo_u32 v29, v123, s14
	v_and_b32_e32 v27, 12, v27
	s_cselect_b32 s0, 0, s8
	s_cselect_b32 s1, s9, s10
	s_lshl_b32 s15, s7, 6
	v_lshlrev_b32_e32 v32, 2, v1
	v_add3_u32 v127, 0, v29, v102
	v_mul_lo_u32 v29, v125, s14
	v_lshl_or_b32 v39, v28, 4, v27
	v_mov_b32_e32 v28, s0
	s_add_i32 s0, s5, s15
	v_and_b32_e32 v41, 48, v1
	s_lshl_b32 s62, s16, 4
	v_add_u32_e32 v119, s4, v32
	v_add3_u32 v128, 0, v29, v102
	v_add_u32_e32 v102, s0, v41
	s_add_i32 s4, s4, s15
	s_and_b32 s0, s62, 16
	v_add_u32_e32 v53, -1, v37
	v_and_b32_e32 v31, 31, v26
	v_lshrrev_b32_e32 v36, 5, v1
	v_add_u32_e32 v131, s4, v41
	s_lshl_b32 s4, s0, 2
	v_cmp_lt_i32_e32 vcc, v53, v38
	v_add_u32_e32 v121, s6, v32
	v_lshlrev_b32_e32 v46, 1, v31
	s_add_i32 s6, s6, s4
	v_lshlrev_b32_e32 v31, 4, v36
	v_cndmask_b32_e32 v53, v53, v37, vcc
	s_lshl_b32 s8, s7, 4
	v_add_u32_e32 v134, s6, v31
	v_cmp_eq_u32_e64 s[6:7], 0, v26
	v_lshlrev_b32_e32 v138, 2, v53
	v_add_u32_e32 v53, -2, v37
	v_writelane_b32 v254, s6, 18
	v_cmp_lt_i32_e32 vcc, v53, v38
	v_lshrrev_b32_e32 v35, 4, v1
	v_writelane_b32 v254, s7, 19
	v_cndmask_b32_e32 v53, v53, v37, vcc
	v_cmp_gt_u32_e64 s[6:7], 2, v1
	v_lshlrev_b32_e32 v139, 2, v53
	v_add_u32_e32 v53, -4, v37
	v_writelane_b32 v254, s6, 24
	v_cmp_lt_i32_e32 vcc, v53, v38
	v_lshlrev_b32_e32 v40, 2, v35
	v_writelane_b32 v254, s7, 25
	v_cmp_gt_u32_e64 s[6:7], 4, v1
	v_cndmask_b32_e32 v53, v53, v37, vcc
	v_lshlrev_b32_e32 v140, 2, v53
	v_writelane_b32 v254, s6, 26
	v_add_u32_e32 v53, -8, v37
	v_cmp_lt_i32_e32 vcc, v53, v38
	v_writelane_b32 v254, s7, 27
	v_cmp_gt_u32_e64 s[6:7], 8, v1
	v_cndmask_b32_e32 v53, v53, v37, vcc
	v_or_b32_e32 v133, s8, v40
	v_writelane_b32 v254, s6, 28
	v_lshlrev_b32_e32 v141, 2, v53
	v_add_u32_e32 v53, -16, v37
	v_writelane_b32 v254, s7, 29
	v_cmp_gt_u32_e64 s[6:7], 32, v1
	v_cmp_lt_i32_e32 vcc, v53, v38
	s_and_b32 s63, s20, 0xffffffc0
	v_writelane_b32 v254, s6, 30
	v_cndmask_b32_e32 v53, v53, v37, vcc
	v_lshlrev_b32_e32 v42, 2, v117
	v_writelane_b32 v254, s7, 31
	v_cmp_gt_u32_e64 s[6:7], v133, v117
	s_add_i32 s64, s63, s3
	v_lshlrev_b32_e32 v142, 2, v53
	v_writelane_b32 v254, s6, 42
	v_subrev_u32_e32 v53, 32, v37
	v_add_u32_e32 v132, s5, v42
	v_writelane_b32 v254, s7, 43
	v_cmp_lt_u32_e64 s[6:7], v133, v117
	v_add_u32_e32 v136, s64, v42
	v_cmp_lt_i32_e32 vcc, v53, v38
	v_add_u32_e32 v38, s1, v42
	v_writelane_b32 v254, s6, 44
	v_or_b32_e32 v42, 2, v133
	v_cndmask_b32_e32 v37, v53, v37, vcc
	v_writelane_b32 v254, s7, 45
	v_cmp_gt_u32_e64 s[6:7], v42, v117
	v_or_b32_e32 v53, 3, v133
	v_or_b32_e32 v147, 16, v117
	v_writelane_b32 v254, s6, 46
	v_or_b32_e32 v148, 32, v117
	v_or_b32_e32 v27, s8, v117
	v_writelane_b32 v254, s7, 47
	v_cmp_lt_u32_e64 s[6:7], v42, v117
	v_or_b32_e32 v48, s62, v117
	v_add_u32_e32 v120, s5, v32
	v_writelane_b32 v254, s6, 48
	v_mad_u32_u24 v28, v27, s14, v28
	v_mul_lo_u32 v27, v48, s14
	v_writelane_b32 v254, s7, 49
	v_cmp_gt_u32_e64 s[6:7], v53, v117
	s_add_i32 s5, s63, s10
	v_add_u32_e32 v135, s5, v27
	v_writelane_b32 v254, s6, 50
	v_lshlrev_b32_e32 v27, 1, v26
	v_and_b32_e32 v27, 62, v27
	v_writelane_b32 v254, s7, 51
	v_cmp_lt_u32_e64 s[6:7], v53, v117
	v_add_u32_e32 v122, s2, v32
	v_add_u32_e32 v34, s64, v32
	v_writelane_b32 v254, s6, 52
	v_lshl_add_u32 v32, v27, 2, s3
	s_lshr_b32 s3, s20, 1
	v_writelane_b32 v254, s7, 53
	v_cmp_gt_u32_e64 s[6:7], v133, v147
	v_lshlrev_b32_e32 v43, 2, v36
	s_and_b32 s3, s3, 0xc0
	v_writelane_b32 v254, s6, 54
	v_or_b32_e32 v45, s0, v43
	s_add_i32 s3, s3, 0
	v_writelane_b32 v254, s7, 55
	v_cmp_lt_u32_e64 s[6:7], v133, v147
	s_lshl_b32 s0, s0, 1
	v_or_b32_e32 v149, 48, v117
	v_writelane_b32 v254, s6, 56
	s_add_i32 s3, s3, s0
	v_lshlrev_b32_e32 v36, 3, v36
	v_writelane_b32 v254, s7, 57
	v_cmp_gt_u32_e64 s[6:7], v42, v147
	v_add_u32_e32 v137, s3, v36
	s_ashr_i32 s3, s20, 3
	v_writelane_b32 v254, s6, 58
	s_movk_i32 s5, 0xffe0
	s_and_b32 s19, s3, 0xffffffe0
	v_writelane_b32 v254, s7, 59
	v_cmp_lt_u32_e64 s[6:7], v42, v147
	v_mov_b32_e32 v52, s3
	s_and_b32 s3, s20, 0x80
	v_writelane_b32 v254, s6, 60
	v_bfi_b32 v52, s5, v52, v26
	s_or_b32 s3, s4, s3
	v_writelane_b32 v254, s7, 61
	v_cmp_gt_u32_e64 s[6:7], v53, v147
	v_mul_lo_u32 v52, v52, s14
	s_add_i32 s3, s3, s9
	v_writelane_b32 v254, s6, 62
	v_add_u32_e32 v52, s3, v52
	s_ashr_i32 s1, s20, 7
; __device__ __forceinline__ void p3_prep(Frame& F) {
;     ...
;         { const bool isq = w >= 4; const int rt = w & 3; const LAS bf16_t* X = isq ? Qs : Ks; LAS float* OUT = isq ? QKm : Am;
;           bf16x8 af[4], bfr[4][4];
; #pragma unroll
;           for (int ks = 0; ks < 4; ++ks) af[ks] = *(const LAS bf16x8*)(X + (rt * 16 + l15) * QP + 32 * ks + 8 * l4);
; #pragma unroll
;           for (int st = 0; st < 4; ++st)
; #pragma unroll
;               for (int ks = 0; ks < 4; ++ks) bfr[st][ks] = *(const LAS bf16x8*)(Ks + (st * 16 + l15) * QP + 32 * ks + 8 * l4);
;           const f32x4 gcr4 = *(const LAS f32x4*)(gc_s + rt * 16 + 4 * l4), br4 = *(const LAS f32x4*)(beta_s + rt * 16 + 4 * l4);
;           float gcs4[4];
; #pragma unroll
;           for (int st = 0; st < 4; ++st) gcs4[st] = gc_s[st * 16 + l15];
; #pragma unroll
;           for (int st = 0; st < 4; ++st) { f32x4 acc = {0.f, 0.f, 0.f, 0.f};
; #pragma unroll
;               for (int ks = 0; ks < 4; ++ks) acc = MFMA16(af[ks], bfr[st][ks], acc);
;               const int sidx = st * 16 + l15; const float gcs = gcs4[st];
; #pragma unroll
;               for (int reg = 0; reg < 4; ++reg) { const int ridx = rt * 16 + 4 * l4 + reg; const float gcr = gcr4[reg], br = br4[reg];
;                   const float e = __expf(fminf(gcr - gcs, 0.f));
;                   const float val = isq ? (ridx >= sidx ? acc[reg] * e : 0.f) : (ridx > sidx ? br * acc[reg] * e : 0.f);
;                   OUT[ridx * FP + sidx] = val; } } }
; #pragma unroll
;         for (int q2 = 0; q2 < 2; ++q2) { const int frag = w + 8 * q2;
;             { const int mt = frag >> 3, kt = (frag >> 1) & 3, s2 = frag & 1, row = 32 * mt + r31, col0 = 32 * kt + 16 * s2 + 4 * hh; const float e = egc_s[row];
;               const u32x2 lo = *(const LAS u32x2*)(Qs + row * QP + col0), hi = *(const LAS u32x2*)(Qs + row * QP + col0 + 8);
;               *(u32x4*)(ub + UO_QD + frag * 1024 + lane * 16) = (u32x4){pk(bf_lo(lo.x) * e, bf_hi(lo.x) * e), pk(bf_lo(lo.y) * e, bf_hi(lo.y) * e), pk(bf_lo(hi.x) * e, bf_hi(hi.x) * e), pk(bf_lo(hi.y) * e, bf_hi(hi.y) * e)}; }
;             { const int kt = frag >> 2, ct = (frag >> 1) & 1, s2 = frag & 1; float v[8];
; #pragma unroll
;               for (int j = 0; j < 8; ++j) { const int tok = 32 * ct + 16 * s2 + 8 * (j >> 2) + 4 * hh + (j & 3); v[j] = bf2f(Ks[tok * QP + 32 * kt + r31]); }
	v_writelane_b32 v254, s7, 63
	v_cmp_lt_u32_e64 s[6:7], v53, v147
	s_lshl_b32 s3, s16, 2
	v_add_u32_e32 v47, 0, v46
	v_writelane_b32 v255, s6, 0
	s_lshl_b32 s17, s16, 11
	s_lshl_b32 s21, s16, 10
	v_writelane_b32 v255, s7, 1
	v_cmp_gt_u32_e64 s[6:7], v133, v148
	s_add_i32 s23, 0, 0x1a000
	s_ashr_i32 s18, s17, 31
	v_writelane_b32 v255, s6, 2
	s_ashr_i32 s22, s21, 31
	v_add_u32_e32 v49, s10, v41
	v_writelane_b32 v255, s7, 3
	v_cmp_lt_u32_e64 s[6:7], v133, v148
	v_or_b32_e32 v50, s62, v40
	v_and_b32_e32 v29, 48, v26
	v_writelane_b32 v255, s6, 4
	v_cmp_eq_u32_e32 vcc, 1, v1
	v_or_b32_e32 v43, s19, v43
	v_writelane_b32 v255, s7, 5
	v_cmp_gt_u32_e64 s[6:7], v42, v148
	v_cndmask_b32_e64 v157, 0, 1.0, vcc
	v_cmp_eq_u32_e32 vcc, 2, v1
	v_writelane_b32 v255, s6, 6
	v_lshlrev_b32_e32 v51, 1, v50
	v_cndmask_b32_e64 v158, 0, 1.0, vcc
	v_writelane_b32 v255, s7, 7
	v_cmp_lt_u32_e64 s[6:7], v42, v148
	v_cmp_eq_u32_e32 vcc, 3, v1
	v_mul_lo_u32 v180, v50, s14
	v_writelane_b32 v255, s6, 8
	v_mul_lo_u32 v43, v43, s14
	v_cndmask_b32_e64 v159, 0, 1.0, vcc
	v_writelane_b32 v255, s7, 9
	v_cmp_gt_u32_e64 s[6:7], v53, v148
	v_cmp_eq_u32_e32 vcc, 4, v1
	s_movk_i32 s24, 0x90
	v_writelane_b32 v255, s6, 10
	v_cndmask_b32_e64 v160, 0, 1.0, vcc
	v_cmp_eq_u32_e32 vcc, 5, v1
	v_writelane_b32 v255, s7, 11
	v_cmp_lt_u32_e64 s[6:7], v53, v148
	v_cndmask_b32_e64 v161, 0, 1.0, vcc
	v_cmp_eq_u32_e32 vcc, 6, v1
	v_writelane_b32 v255, s6, 12
	v_mul_lo_u32 v48, v48, s24
	v_cndmask_b32_e64 v163, 0, 1.0, vcc
	v_writelane_b32 v255, s7, 13
	v_cmp_gt_u32_e64 s[6:7], v133, v149
	v_cmp_eq_u32_e32 vcc, 7, v1
	v_add_u32_e32 v48, 0, v48
	v_writelane_b32 v255, s6, 14
	v_cndmask_b32_e64 v164, 0, 1.0, vcc
	v_cmp_eq_u32_e32 vcc, 8, v1
	v_writelane_b32 v255, s7, 15
	v_cmp_lt_u32_e64 s[6:7], v133, v149
	v_cndmask_b32_e64 v165, 0, 1.0, vcc
	v_cmp_eq_u32_e32 vcc, 9, v1
	v_writelane_b32 v255, s6, 16
	v_lshlrev_b32_e32 v143, 2, v37
	v_cndmask_b32_e64 v166, 0, 1.0, vcc
	v_writelane_b32 v255, s7, 17
	v_cmp_gt_u32_e64 s[6:7], v42, v149
	v_cmp_eq_u32_e32 vcc, 10, v1
	v_mul_u32_u24_e32 v37, 0x240, v117
	v_writelane_b32 v255, s6, 18
	v_cndmask_b32_e64 v167, 0, 1.0, vcc
	v_cmp_eq_u32_e32 vcc, 11, v1
	v_writelane_b32 v255, s7, 19
	v_cmp_lt_u32_e64 s[6:7], v42, v149
	v_mov_b32_e32 v42, s3
	s_lshl_b32 s3, s1, 6
	s_and_b32 s1, s1, 1
	s_and_b32 s3, s3, 0xc0
	v_lshl_or_b32 v54, s1, 5, v45
	s_lshl_b32 s1, s1, 7
	v_bfi_b32 v42, s5, v42, v26
	s_or_b32 s3, s0, s3
	v_writelane_b32 v254, s1, 32
	s_add_i32 s1, s16, 8
	v_mul_lo_u32 v152, v42, s14
	s_add_i32 s3, s3, 0
	s_lshl_b32 s4, s1, 2
	v_add3_u32 v153, s3, v152, v36
	s_and_b32 s3, s62, 0xffffffc0
	v_mov_b32_e32 v55, s4
	v_lshl_add_u32 v151, v42, 2, s2
	v_add_u32_e32 v42, s3, v47
	s_ashr_i32 s3, s1, 1
	v_bfi_b32 v55, s5, v55, v26
	v_lshl_add_u32 v154, v55, 2, s2
	s_lshl_b32 s2, s3, 6
	s_and_b32 s2, s2, 0xc0
	s_or_b32 s0, s0, s2
	v_mul_lo_u32 v155, v55, s14
	s_add_i32 s0, s0, 0
	v_add3_u32 v156, s0, v155, v36
	s_lshl_b32 s70, s1, 10
	s_and_b32 s0, s3, 1
	s_lshl_b32 s1, s1, 4
	s_ashr_i32 s25, s70, 31
	s_andn2_b32 s1, s1, 63
	v_lshl_or_b32 v45, s0, 5, v45
	s_lshl_b32 s0, s0, 7
	s_cmp_lt_i32 s16, 3
	v_add_u32_e32 v36, s1, v47
	v_writelane_b32 v254, s0, 34
	s_cselect_b64 s[0:1], -1, 0
	v_writelane_b32 v254, s0, 36
	v_writelane_b32 v255, s6, 20
	v_cndmask_b32_e64 v168, 0, 1.0, vcc
	v_writelane_b32 v254, s1, 37
	s_add_i32 s0, s62, 16
	s_cmp_lt_i32 s16, 2
	v_or_b32_e32 v47, s0, v117
	v_or_b32_e32 v55, s0, v40
	s_cselect_b64 s[0:1], -1, 0
	v_writelane_b32 v254, s0, 20
	v_writelane_b32 v255, s7, 21
	v_cmp_gt_u32_e64 s[6:7], v53, v149
	v_writelane_b32 v254, s1, 21
	s_add_i32 s0, s62, 32
	s_cmp_lt_i32 s16, 1
	v_or_b32_e32 v56, s0, v117
	v_or_b32_e32 v57, s0, v40
	s_cselect_b64 s[0:1], -1, 0
	v_writelane_b32 v255, s6, 22
	v_writelane_b32 v254, s0, 22
	v_mul_lo_u32 v47, v47, s14
	v_writelane_b32 v255, s7, 23
	v_writelane_b32 v254, s1, 23
	v_cmp_lt_u32_e64 s[0:1], v53, v149
	v_add3_u32 v173, v49, v47, s63
	v_add3_u32 v176, s64, v47, v41
; __device__ __forceinline__ void p3_prep(Frame& F) {
;     ...
;     for (int uid = F.bid; uid < NUNITS; uid += F.G) {
;         unsigned char* ub = F.ws + WS_PREP + (size_t)uid * UNIT_BYTES;
;         float gc = pg; const float beta = pb;
; #pragma unroll
;         for (int off = 1; off < 64; off <<= 1) { const float t = __shfl_up(gc, off); if (lane >= off) gc += t; }
;         const float glast = __shfl(gc, 63), egcv = __expf(gc);
;         if (w == 0) { egc_s[lane] = egcv; ekd_s[lane] = __expf(glast - gc); gc_s[lane] = gc; beta_s[lane] = beta; }
;         { const int r0 = 2 * (tid >> 4), c16 = tid & 15;
;           const float br0 = __shfl(beta, r0), br1 = __shfl(beta, r0 + 1), sk0 = br0 * __shfl(egcv, r0), sk1 = br1 * __shfl(egcv, r0 + 1);
;           const int rs = (((r0 >> 3) ^ (c16 >> 1)) << 3) + (r0 & 7);
;           *(LAS u32x4*)(Qs + r0 * QP + c16 * 8) = pre[0][0]; *(LAS u32x4*)(Qs + (r0 + 1) * QP + c16 * 8) = pre[0][1];
;           *(LAS u32x4*)(Ks + r0 * QP + c16 * 8) = pre[1][0]; *(LAS u32x4*)(Ks + (r0 + 1) * QP + c16 * 8) = pre[1][1];
; #pragma unroll
;           for (int e = 0; e < 4; ++e) { const unsigned k0 = pre[1][0][e], k1 = pre[1][1][e], v0 = pre[2][0][e], v1 = pre[2][1][e];
;               *(LAS unsigned*)(KbgT + (c16 * 8 + 2 * e) * TP + rs) = pk(bf_lo(k0) * sk0, bf_lo(k1) * sk1); *(LAS unsigned*)(KbgT + (c16 * 8 + 2 * e + 1) * TP + rs) = pk(bf_hi(k0) * sk0, bf_hi(k1) * sk1);
;               *(LAS unsigned*)(VbT + (c16 * 8 + 2 * e) * TP + rs) = pk(bf_lo(v0) * br0, bf_lo(v1) * br1); *(LAS unsigned*)(VbT + (c16 * 8 + 2 * e + 1) * TP + rs) = pk(bf_hi(v0) * br0, bf_hi(v1) * br1); } }
;         if (uid + F.G < NUNITS) PREP_LOAD(uid + F.G);
;         __syncthreads();
;         { const bool isq = w >= 4; const int rt = w & 3; const LAS bf16_t* X = isq ? Qs : Ks; LAS float* OUT = isq ? QKm : Am;
;           bf16x8 af[4], bfr[4][4];
; #pragma unroll
;           for (int ks = 0; ks < 4; ++ks) af[ks] = *(const LAS bf16x8*)(X + (rt * 16 + l15) * QP + 32 * ks + 8 * l4);
; #pragma unroll
;           for (int st = 0; st < 4; ++st)
; #pragma unroll
;               for (int ks = 0; ks < 4; ++ks) bfr[st][ks] = *(const LAS bf16x8*)(Ks + (st * 16 + l15) * QP + 32 * ks + 8 * l4);
;           const f32x4 gcr4 = *(const LAS f32x4*)(gc_s + rt * 16 + 4 * l4), br4 = *(const LAS f32x4*)(beta_s + rt * 16 + 4 * l4);
;           float gcs4[4];
; #pragma unroll
	v_writelane_b32 v255, s0, 24
	v_ashrrev_i32_e32 v47, 5, v26
	v_cmp_gt_i32_e64 s[2:3], v27, v47
	v_writelane_b32 v255, s1, 25
	v_cmp_eq_u32_e64 s[0:1], 0, v1
	s_add_i32 s62, s62, 48
	v_or_b32_e32 v58, s62, v117
	v_writelane_b32 v253, s0, 21
	v_mul_lo_u32 v56, v56, s14
	v_mul_lo_u32 v58, v58, s14
	v_writelane_b32 v253, s1, 22
	v_writelane_b32 v253, s2, 23
	s_add_i32 s15, s15, 0
	v_add3_u32 v174, v49, v56, s63
	v_writelane_b32 v253, s3, 24
	v_cmp_lt_i32_e64 s[2:3], v27, v47
	v_add3_u32 v175, v49, v58, s63
	v_mul_u32_u24_e32 v49, 0x110, v54
	v_writelane_b32 v253, s2, 26
	v_add3_u32 v178, s64, v58, v41
	v_cndmask_b32_e64 v179, 0, 1.0, s[0:1]
	v_writelane_b32 v253, s3, 27
	s_mul_i32 s2, s80, 0x12400
	v_add_u32_e32 v54, 0x200, v26
	v_add_u32_e32 v58, 0x400, v26
	v_add_u32_e32 v26, 0x600, v26
	s_mul_hi_i32 s1, s80, 0x12400
	s_add_u32 s2, s86, s2
	v_or_b32_e32 v40, s62, v40
	v_ashrrev_i32_e32 v54, 5, v54
	v_ashrrev_i32_e32 v58, 5, v58
	v_ashrrev_i32_e32 v26, 5, v26
	v_mul_lo_u32 v182, v57, s14
	v_mul_u32_u24_e32 v57, 0x90, v117
	s_addc_u32 s1, s87, s1
	v_add3_u32 v177, s64, v56, v41
	v_mul_lo_u32 v181, v55, s14
	v_mul_lo_u32 v40, v40, s14
	v_mul_lo_u32 v50, v47, s14
	v_add3_u32 v183, s23, v57, v41
	v_mul_lo_u32 v41, v54, s14
	v_mul_lo_u32 v57, v58, s14
	v_mul_lo_u32 v61, v26, s14
	s_add_u32 s14, s2, 0x46212000
	v_cmp_gt_i32_e64 s[2:3], v27, v54
	s_mul_i32 s0, s16, 0x1100
	v_add3_u32 v184, s15, v43, v46
	v_writelane_b32 v253, s2, 28
	s_addc_u32 s15, s1, 0
	v_add_u32_e32 v198, s0, v34
	v_writelane_b32 v253, s3, 29
	v_writelane_b32 v253, s80, 45
	v_cmp_lt_i32_e64 s[0:1], v27, v54
	v_cmp_eq_u32_e32 vcc, 12, v1
	v_xor_b32_e32 v55, s16, v35
	v_writelane_b32 v253, s0, 30
	v_bitop3_b32 v35, v35, s16, 4 bitop3:0x36
	v_cndmask_b32_e64 v169, 0, 1.0, vcc
	v_writelane_b32 v253, s1, 31
	v_cmp_gt_i32_e64 s[0:1], v27, v58
	v_cmp_eq_u32_e32 vcc, 13, v1
	v_lshl_add_u32 v186, v35, 4, v48
	v_writelane_b32 v253, s0, 56
	v_mul_u32_u24_e32 v35, 0x88, v117
	v_lshlrev_b32_e32 v37, 1, v37
	v_writelane_b32 v253, s1, 57
	v_cmp_lt_i32_e64 s[0:1], v27, v58
	v_cndmask_b32_e64 v170, 0, 1.0, vcc
	v_cmp_eq_u32_e32 vcc, 14, v1
	v_writelane_b32 v253, s0, 39
	v_lshlrev_b32_e32 v35, 1, v35
	v_add_u32_e32 v30, 0, v29
	v_writelane_b32 v253, s1, 40
	v_cmp_gt_i32_e64 s[0:1], v27, v26
	v_lshlrev_b32_e32 v44, 4, v1
	v_lshl_add_u32 v33, v27, 1, s23
	v_writelane_b32 v253, s0, 37
	v_add3_u32 v144, 0, v39, v37
	v_mul_u32_u24_e32 v37, 0x110, v117
	v_writelane_b32 v253, s1, 38
	v_cmp_lt_i32_e64 s[0:1], v27, v26
	v_mul_u32_u24_e32 v39, 0x110, v133
	v_cndmask_b32_e64 v171, 0, 1.0, vcc
	v_cmp_eq_u32_e32 vcc, 15, v1
	v_mul_u32_u24_e32 v45, 0x110, v45
	v_mul_lo_u32 v53, v47, s24
	v_mul_lo_u32 v56, v54, s24
	v_mul_lo_u32 v59, v58, s24
	v_mul_lo_u32 v60, v26, s24
	v_add3_u32 v187, 0, v51, v35
	v_writelane_b32 v253, s0, 52
	v_writelane_b32 v255, s26, 26
	v_cmp_gt_u32_e64 s[48:49], 16, v1
	v_sub_u32_e32 v145, 63, v123
	v_sub_u32_e32 v146, 63, v125
	v_or_b32_e32 v150, 1, v133
	v_cndmask_b32_e64 v172, 0, 1.0, vcc
	v_or_b32_e32 v106, s21, v44
	v_mov_b32_e32 v107, s22
	v_or_b32_e32 v108, s70, v44
	v_lshl_add_u32 v185, v55, 4, v48
	v_add_u32_e32 v188, 0x900, v183
	v_add_u32_e32 v189, 0x1100, v187
	v_add_u32_e32 v190, 0x1200, v183
	v_add_u32_e32 v191, 0x2200, v187
	v_add_u32_e32 v192, 0x1b00, v183
	v_add_u32_e32 v193, 0x3300, v187
	v_mov_b32_e32 v109, s25
	v_lshl_or_b32 v110, v1, 5, s17
	v_mov_b32_e32 v111, s18
	v_add_u32_e32 v194, v28, v29
	v_add_u32_e32 v195, v30, v37
	v_add_u32_e32 v196, v42, v49
	v_add_u32_e32 v197, v36, v45
	v_add_u32_e32 v199, v136, v40
	v_add_u32_e32 v200, v32, v50
	v_add_u32_e32 v201, v33, v53
	v_add_u32_e32 v202, v32, v41
	v_add_u32_e32 v203, v33, v56
	v_add_u32_e32 v204, v32, v57
	v_add_u32_e32 v205, v33, v59
	v_add_u32_e32 v206, v32, v61
	v_add_u32_e32 v207, v33, v60
	v_add_u32_e32 v208, v52, v31
	v_add_u32_e32 v209, v38, v39
	v_writelane_b32 v253, s1, 53
	v_writelane_b32 v255, s27, 27
	s_waitcnt vmcnt(0)
	s_branch .LBB0_487

; #define LAS __attribute__((address_space(3)))
; __device__ __forceinline__ float bf_lo(unsigned w) { return __uint_as_float(w << 16); }
; __device__ __forceinline__ float bf_hi(unsigned w) { return __uint_as_float(w & 0xffff0000u); }
; __device__ __forceinline__ unsigned pk(float a, float b) { f32x2 v = {a, b}; return __builtin_bit_cast(unsigned, __builtin_convertvector(v, bf2_t)); }
; __device__ __forceinline__ void p3_prep(Frame& F) {
;     ...
;         float gc = pg; const float beta = pb;
; #pragma unroll
;         for (int off = 1; off < 64; off <<= 1) { const float t = __shfl_up(gc, off); if (lane >= off) gc += t; }
;         const float glast = __shfl(gc, 63), egcv = __expf(gc);
;         if (w == 0) { egc_s[lane] = egcv; ekd_s[lane] = __expf(glast - gc); gc_s[lane] = gc; beta_s[lane] = beta; }
;         { const int r0 = 2 * (tid >> 4), c16 = tid & 15;
;           const float br0 = __shfl(beta, r0), br1 = __shfl(beta, r0 + 1), sk0 = br0 * __shfl(egcv, r0), sk1 = br1 * __shfl(egcv, r0 + 1);
;           const int rs = (((r0 >> 3) ^ (c16 >> 1)) << 3) + (r0 & 7);
;           *(LAS u32x4*)(Qs + r0 * QP + c16 * 8) = pre[0][0]; *(LAS u32x4*)(Qs + (r0 + 1) * QP + c16 * 8) = pre[0][1];
;           *(LAS u32x4*)(Ks + r0 * QP + c16 * 8) = pre[1][0]; *(LAS u32x4*)(Ks + (r0 + 1) * QP + c16 * 8) = pre[1][1];
; #pragma unroll
;           for (int e = 0; e < 4; ++e) { const unsigned k0 = pre[1][0][e], k1 = pre[1][1][e], v0 = pre[2][0][e], v1 = pre[2][1][e];
;               *(LAS unsigned*)(KbgT + (c16 * 8 + 2 * e) * TP + rs) = pk(bf_lo(k0) * sk0, bf_lo(k1) * sk1); *(LAS unsigned*)(KbgT + (c16 * 8 + 2 * e + 1) * TP + rs) = pk(bf_hi(k0) * sk0, bf_hi(k1) * sk1);
;               *(LAS unsigned*)(VbT + (c16 * 8 + 2 * e) * TP + rs) = pk(bf_lo(v0) * br0, bf_lo(v1) * br1); *(LAS unsigned*)(VbT + (c16 * 8 + 2 * e + 1) * TP + rs) = pk(bf_hi(v0) * br0, bf_hi(v1) * br1); } }
.LBB0_487:
	s_waitcnt vmcnt(10)
	ds_bpermute_b32 v26, v138, v130
	v_readlane_b32 s0, v253, 21
	v_readlane_b32 s1, v253, 22
	s_waitcnt lgkmcnt(0)
	v_add_f32_e32 v26, v130, v26
	v_cndmask_b32_e64 v26, v26, v130, s[0:1]
	ds_bpermute_b32 v27, v139, v26
	v_readlane_b32 s0, v254, 24
	v_readlane_b32 s1, v254, 25
	s_waitcnt lgkmcnt(0)
	v_add_f32_e32 v27, v26, v27
	v_cndmask_b32_e64 v26, v27, v26, s[0:1]
	ds_bpermute_b32 v27, v140, v26
	v_readlane_b32 s0, v254, 26
	v_readlane_b32 s1, v254, 27
	s_waitcnt lgkmcnt(0)
	v_add_f32_e32 v27, v26, v27
	v_cndmask_b32_e64 v26, v27, v26, s[0:1]
	ds_bpermute_b32 v27, v141, v26
	v_readlane_b32 s0, v254, 28
	v_readlane_b32 s1, v254, 29
	s_waitcnt lgkmcnt(0)
	v_add_f32_e32 v27, v26, v27
	v_cndmask_b32_e64 v26, v27, v26, s[0:1]
	ds_bpermute_b32 v27, v142, v26
	v_readlane_b32 s0, v254, 30
	v_readlane_b32 s1, v254, 31
	s_waitcnt lgkmcnt(0)
	v_add_f32_e32 v27, v26, v27
	v_cndmask_b32_e64 v26, v27, v26, s[48:49]
	ds_bpermute_b32 v27, v143, v26
	s_waitcnt lgkmcnt(0)
	v_add_f32_e32 v27, v26, v27
	v_cndmask_b32_e64 v27, v27, v26, s[0:1]
	ds_bpermute_b32 v210, v118, v27
	v_mul_f32_e32 v26, 0x3fb8aa3b, v27
	v_exp_f32_e32 v26, v26
	v_readlane_b32 s0, v254, 16
	v_readlane_b32 s1, v254, 17
	s_andn2_b64 vcc, exec, s[0:1]
	s_cbranch_vccnz .LBB0_489
	s_waitcnt lgkmcnt(0)
	v_sub_f32_e32 v28, v210, v27
	v_mul_f32_e32 v28, 0x3fb8aa3b, v28
	v_exp_f32_e32 v28, v28
	ds_write_b32 v122, v26
	ds_write_b32 v120, v27
	ds_write_b32 v121, v28
	s_waitcnt vmcnt(9)
	ds_write_b32 v119, v129
.LBB0_489:
	s_waitcnt vmcnt(9)
	ds_bpermute_b32 v28, v124, v129
	ds_bpermute_b32 v31, v126, v129
	ds_bpermute_b32 v30, v124, v26
	ds_bpermute_b32 v29, v126, v26
	v_lshlrev_b32_e32 v33, 16, v14
	v_lshlrev_b32_e32 v32, 16, v6
	v_add_u32_e32 v34, 0x8800, v144
	ds_write_b128 v127, v[2:5]
	ds_write_b128 v128, v[10:13]
	ds_write_b128 v127, v[6:9] offset:17408
	ds_write_b128 v128, v[14:17] offset:17408
	s_waitcnt lgkmcnt(4)
	v_pk_mul_f32 v[26:27], v[30:31], v[28:29]
	v_readlane_b32 s0, v253, 45
	v_pk_mul_f32 v[32:33], v[26:27], v[32:33]
	s_add_i32 s0, s0, s79
	v_cvt_pk_bf16_f32 v29, v32, v33
	v_and_b32_e32 v33, 0xffff0000, v14
	v_and_b32_e32 v32, 0xffff0000, v6
	v_pk_mul_f32 v[32:33], v[26:27], v[32:33]
	s_cmpk_gt_i32 s0, 0x107f
	v_cvt_pk_bf16_f32 v30, v32, v33
	ds_write2_b32 v34, v29, v30 offset1:36
	v_lshlrev_b32_e32 v33, 16, v22
	v_lshlrev_b32_e32 v32, 16, v18
	v_mov_b32_e32 v29, v31
	v_pk_mul_f32 v[30:31], v[32:33], v[28:29]
	v_add_u32_e32 v33, 0xd000, v144
	v_cvt_pk_bf16_f32 v32, v30, v31
	v_and_b32_e32 v31, 0xffff0000, v22
	v_and_b32_e32 v30, 0xffff0000, v18
	v_pk_mul_f32 v[30:31], v[30:31], v[28:29]
	v_writelane_b32 v253, s0, 45
	v_cvt_pk_bf16_f32 v30, v30, v31
	ds_write2_b32 v33, v32, v30 offset1:36
	v_lshlrev_b32_e32 v31, 16, v15
	v_lshlrev_b32_e32 v30, 16, v7
	v_pk_mul_f32 v[30:31], v[26:27], v[30:31]
	s_cselect_b64 s[0:1], -1, 0
	v_cvt_pk_bf16_f32 v32, v30, v31
	v_and_b32_e32 v31, 0xffff0000, v15
	v_and_b32_e32 v30, 0xffff0000, v7
	v_pk_mul_f32 v[30:31], v[26:27], v[30:31]
	v_writelane_b32 v254, s0, 12
	v_cvt_pk_bf16_f32 v30, v30, v31
	ds_write2_b32 v34, v32, v30 offset0:72 offset1:108
	v_lshlrev_b32_e32 v31, 16, v23
	v_lshlrev_b32_e32 v30, 16, v19
	v_pk_mul_f32 v[30:31], v[30:31], v[28:29]
	v_writelane_b32 v254, s1, 13
	v_cvt_pk_bf16_f32 v32, v30, v31
	v_and_b32_e32 v31, 0xffff0000, v23
	v_and_b32_e32 v30, 0xffff0000, v19
	v_pk_mul_f32 v[30:31], v[30:31], v[28:29]
	s_and_b64 vcc, exec, s[0:1]
	v_cvt_pk_bf16_f32 v30, v30, v31
	ds_write2_b32 v33, v32, v30 offset0:72 offset1:108
	v_lshlrev_b32_e32 v31, 16, v16
	v_lshlrev_b32_e32 v30, 16, v8
	v_pk_mul_f32 v[30:31], v[26:27], v[30:31]
	s_nop 0
	v_cvt_pk_bf16_f32 v32, v30, v31
	v_and_b32_e32 v31, 0xffff0000, v16
	v_and_b32_e32 v30, 0xffff0000, v8
	v_pk_mul_f32 v[30:31], v[26:27], v[30:31]
	s_nop 0
	v_cvt_pk_bf16_f32 v30, v30, v31
	ds_write2_b32 v34, v32, v30 offset0:144 offset1:180
	v_lshlrev_b32_e32 v31, 16, v24
	v_lshlrev_b32_e32 v30, 16, v20
	v_pk_mul_f32 v[30:31], v[30:31], v[28:29]
	s_nop 0
	v_cvt_pk_bf16_f32 v32, v30, v31
	v_and_b32_e32 v31, 0xffff0000, v24
	v_and_b32_e32 v30, 0xffff0000, v20
	v_pk_mul_f32 v[30:31], v[30:31], v[28:29]
	s_nop 0
	v_cvt_pk_bf16_f32 v30, v30, v31
	ds_write2_b32 v33, v32, v30 offset0:144 offset1:180
	v_lshlrev_b32_e32 v31, 16, v17
	v_lshlrev_b32_e32 v30, 16, v9
	v_pk_mul_f32 v[30:31], v[26:27], v[30:31]
	s_nop 0
	v_cvt_pk_bf16_f32 v32, v30, v31
	v_and_b32_e32 v31, 0xffff0000, v17
	v_and_b32_e32 v30, 0xffff0000, v9
	v_pk_mul_f32 v[26:27], v[26:27], v[30:31]
	s_nop 0
	v_cvt_pk_bf16_f32 v26, v26, v27
	ds_write2_b32 v34, v32, v26 offset0:216 offset1:252
	v_lshlrev_b32_e32 v27, 16, v25
	v_lshlrev_b32_e32 v26, 16, v21
	v_pk_mul_f32 v[26:27], v[26:27], v[28:29]
	s_nop 0
	v_cvt_pk_bf16_f32 v30, v26, v27
	v_and_b32_e32 v27, 0xffff0000, v25
	v_and_b32_e32 v26, 0xffff0000, v21
	v_pk_mul_f32 v[26:27], v[26:27], v[28:29]
	s_nop 0
	v_cvt_pk_bf16_f32 v26, v26, v27
	ds_write2_b32 v33, v30, v26 offset0:216 offset1:252
	s_cbranch_vccnz .LBB0_495
	v_readlane_b32 s0, v253, 45
	s_ashr_i32 s0, s0, 4
	s_mul_hi_i32 s1, s0, 0x3e0f83e1
	s_lshr_b32 s2, s1, 31
	s_ashr_i32 s1, s1, 5
	s_add_i32 s1, s1, s2
	s_mul_i32 s2, s1, 0x84
	s_sub_i32 s2, s0, s2
	s_cmp_gt_i32 s2, 3
	s_mov_b64 s[18:19], -1
	s_cbranch_scc0 .LBB0_492
	s_lshl_b32 s0, s1, 13
	s_lshl_b32 s3, s2, 6
	s_add_i32 s0, s3, s0
	s_addk_i32 s0, 0xff00
	s_mov_b64 s[18:19], 0
